# E phase: per-column constant loads issued in one batch (one round trip instead of eight)
# speedup vs baseline: 1.0098x; 1.0014x over previous
; __device__ void phase_E_rows(const Params& p, int l, char* smem, int vb, int nvb, bool split, int nrows, int oz) {
;     ...
;         const int mr = isctx ? 8 : row / T;
;         if (mr != cur_mr) {
;             cur_mr = mr;
; #pragma unroll
;             for (int k = 0; k < 4; ++k) {
;                 const int col = (k >> 1) * 512 + lane * 8 + (k & 1) * 4;
;                 if (l > 0) {
;                     const float4 g = *(const float4*)(mod + ((l - 1) * 9 + mr) * 3072 + 2048 + col);
;                     const float4 pg = *(const float4*)(p.in[I_POSTG] + (l - 1) * DM + col);
;                     gp[k] = make_float4(g.x * pg.x, g.y * pg.y, g.z * pg.z, g.w * pg.w);
;                 }
;                 if (l < 4) {
;                     const float4 pre = *(const float4*)(p.in[I_PREG] + l * DM + col);
;                     const float4 sc = *(const float4*)(mod + (l * 9 + mr) * 3072 + 1024 + col);
;                     sh[k] = *(const float4*)(mod + (l * 9 + mr) * 3072 + col);
;                     pa[k] = make_float4(pre.x * (1.f + sc.x), pre.y * (1.f + sc.y), pre.z * (1.f + sc.z), pre.w * (1.f + sc.w));
;                 }
;             }
.LBB0_914:
	s_ashr_i32 s20, s56, 31
	s_lshr_b32 s20, s20, 21
	s_add_i32 s20, s56, s20
	s_ashr_i32 s29, s20, 11
	s_cmpk_gt_i32 s56, 0x3fff
	s_cselect_b64 s[20:21], -1, 0
	s_and_b64 s[46:47], s[20:21], exec
	s_cselect_b32 s66, 8, s29
	v_mov_b64_e32 v[150:151], v[64:65]
	v_mov_b64_e32 v[152:153], v[66:67]
	v_mov_b64_e32 v[154:155], v[60:61]
	v_mov_b64_e32 v[156:157], v[62:63]
	v_mov_b64_e32 v[158:159], v[56:57]
	v_mov_b64_e32 v[160:161], v[58:59]
	v_mov_b64_e32 v[162:163], v[52:53]
	s_cmp_eq_u32 s66, s28
	v_mov_b64_e32 v[164:165], v[54:55]
	s_cbranch_scc1 .LBB0_931
	s_add_i32 s28, s66, s48
	s_mulk_i32 s28, 0xc00
	s_ashr_i32 s29, s28, 31
	s_lshl_b64 s[28:29], s[28:29], 2
	s_add_u32 s28, s60, s28
	s_addc_u32 s29, s61, s29
	s_add_u32 s84, s28, 0x2000
	s_addc_u32 s85, s29, 0
	s_add_i32 s28, s66, s49
	s_mulk_i32 s28, 0xc00
	s_ashr_i32 s29, s28, 31
	s_lshl_b64 s[28:29], s[28:29], 2
	s_add_u32 s28, s60, s28
	s_addc_u32 s29, s61, s29
	s_add_u32 s82, s28, 0x1000
	v_cndmask_b32_e64 v52, 0, 1, s[50:51]
	s_addc_u32 s83, s29, 0
	v_cmp_ne_u32_e64 s[46:47], 1, v52
	v_lshlrev_b32_e32 v56, 2, v106
	v_lshlrev_b32_e32 v57, 2, v108
	v_lshlrev_b32_e32 v58, 2, v110
	s_and_b64 vcc, exec, s[44:45]
	s_cbranch_vccnz .Le_mod_noA
	global_load_dwordx4 v[118:121], v2, s[84:85]
	global_load_dwordx4 v[202:205], v[112:113], off
	global_load_dwordx4 v[122:125], v56, s[84:85]
	global_load_dwordx4 v[206:209], v[112:113], off offset:16
	global_load_dwordx4 v[126:129], v57, s[84:85]
	global_load_dwordx4 v[210:213], v[112:113], off offset:2048
	global_load_dwordx4 v[134:137], v58, s[84:85]
	global_load_dwordx4 v[214:217], v[112:113], off offset:2064
.Le_mod_noA:
	s_andn2_b64 vcc, exec, s[50:51]
	s_cbranch_vccnz .Le_mod_noB
	global_load_dwordx4 v[218:221], v2, s[82:83]
	global_load_dwordx4 v[222:225], v[114:115], off
	global_load_dwordx4 v[4:7], v2, s[28:29]
	global_load_dwordx4 v[226:229], v56, s[82:83]
	global_load_dwordx4 v[230:233], v[114:115], off offset:16
	global_load_dwordx4 v[8:11], v2, s[28:29] offset:16
	global_load_dwordx4 v[184:187], v57, s[82:83]
	global_load_dwordx4 v[188:191], v[114:115], off offset:2048
	global_load_dwordx4 v[12:15], v2, s[28:29] offset:2048
	global_load_dwordx4 v[192:195], v58, s[82:83]
	global_load_dwordx4 v[52:55], v[114:115], off offset:2064
	global_load_dwordx4 v[16:19], v2, s[28:29] offset:2064
.Le_mod_noB:
	s_waitcnt vmcnt(0)
	s_and_b64 vcc, exec, s[44:45]
	s_cbranch_vccnz .Le_mod_cA
	v_pk_mul_f32 v[118:119], v[118:119], v[202:203]
	v_pk_mul_f32 v[120:121], v[120:121], v[204:205]
	v_pk_mul_f32 v[122:123], v[122:123], v[206:207]
	v_pk_mul_f32 v[124:125], v[124:125], v[208:209]
	v_pk_mul_f32 v[126:127], v[126:127], v[210:211]
	v_pk_mul_f32 v[128:129], v[128:129], v[212:213]
	v_pk_mul_f32 v[134:135], v[134:135], v[214:215]
	v_pk_mul_f32 v[136:137], v[136:137], v[216:217]
.Le_mod_cA:
	s_andn2_b64 vcc, exec, s[50:51]
	s_cbranch_vccnz .LBB0_932
	v_pk_add_f32 v[218:219], v[218:219], 1.0 op_sel_hi:[1,0]
	v_pk_add_f32 v[220:221], v[220:221], 1.0 op_sel_hi:[1,0]
	v_pk_mul_f32 v[132:133], v[222:223], v[218:219]
	v_pk_mul_f32 v[130:131], v[224:225], v[220:221]
	v_pk_add_f32 v[226:227], v[226:227], 1.0 op_sel_hi:[1,0]
	v_pk_add_f32 v[228:229], v[228:229], 1.0 op_sel_hi:[1,0]
	v_pk_mul_f32 v[140:141], v[230:231], v[226:227]
	v_pk_mul_f32 v[138:139], v[232:233], v[228:229]
	v_pk_add_f32 v[184:185], v[184:185], 1.0 op_sel_hi:[1,0]
	v_pk_add_f32 v[186:187], v[186:187], 1.0 op_sel_hi:[1,0]
	v_pk_mul_f32 v[144:145], v[188:189], v[184:185]
	v_pk_mul_f32 v[142:143], v[190:191], v[186:187]
	v_pk_add_f32 v[192:193], v[192:193], 1.0 op_sel_hi:[1,0]
	v_pk_add_f32 v[194:195], v[194:195], 1.0 op_sel_hi:[1,0]
	v_pk_mul_f32 v[146:147], v[52:53], v[192:193]
	v_pk_mul_f32 v[148:149], v[54:55], v[194:195]
	s_branch .LBB0_932
